# speedup vs baseline: 1.0182x; 1.0182x over previous
.LBB1_8:
	s_waitcnt lgkmcnt(0)
	v_lshrrev_b32_e32 v7, 5, v2
	v_lshlrev_b32_e64 v9, v2, -2
	s_waitcnt lgkmcnt(0)
	v_and_b32_e32 v9, v9, v6
	v_cmp_eq_u32_e32 vcc, v3, v7
	s_nop 1
	v_cndmask_b32_e32 v9, 0, v9, vcc
	v_cmp_gt_u32_e32 vcc, v3, v7
	s_nop 1
	v_cndmask_b32_e32 v9, v9, v6, vcc
	v_cmp_ne_u32_e32 vcc, 0, v9
	s_and_b32 s3, vcc_lo, 0xffff
	s_cmp_eq_u32 s3, 0
	s_cbranch_scc1 .LBB1_13
	s_ff1_i32_b32 s3, s3
	v_readlane_b32 s15, v9, s3
	s_ff1_i32_b32 s15, s15
	s_lshl_b32 s18, s3, 11
	s_lshl_b32 s15, s15, 6
	s_add_i32 s18, s18, s15
	v_lshl_or_b32 v7, v3, 2, s18
	v_add_u32_e32 v10, -1, v9
	v_cmp_eq_u32_e32 vcc, s3, v3
	ds_read_b32 v7, v7
	v_cndmask_b32_e32 v10, -1, v10, vcc
	v_and_b32_e32 v11, v10, v9
	v_cmp_ne_u32_e32 vcc, 0, v11
	s_and_b32 s3, vcc_lo, 0xffff
	s_cmp_lg_u32 s3, 0
	s_cbranch_scc0 .Lk2_single
	s_ff1_i32_b32 s3, s3
	v_readlane_b32 s15, v11, s3
	s_ff1_i32_b32 s15, s15
	s_lshl_b32 s20, s3, 5
	s_or_b32 s22, s15, s20
	v_lshl_or_b32 v9, s22, 6, v4
	ds_read_b32 v9, v9
	s_waitcnt lgkmcnt(1)
	v_readlane_b32 s3, v7, s3
	s_lshr_b32 s3, s3, s15
	s_bitcmp0_b32 s3, 0
	s_cselect_b64 vcc, -1, 0
	s_waitcnt lgkmcnt(0)
	v_not_b32_e32 v9, v9
	v_cndmask_b32_e32 v9, -1, v9, vcc
	v_bitop3_b32 v9, v9, v6, v7 bitop3:0x40
	v_mov_b32_e32 v2, s22
	v_mov_b32_e32 v6, v9
	s_branch .LBB1_8
.Lk2_single:
	s_waitcnt lgkmcnt(0)
	v_bitop3_b32 v6, v6, v7, v6 bitop3:0x30
	s_branch .LBB1_14
